# conversion store step: 4 LDS reads issued together, stores 2-4 reuse store 1's address plus a scalar row offset
# baseline (speedup 1.0000x reference)
; #define GAS __attribute__((address_space(1)))
; #define LAS __attribute__((address_space(3)))
; __device__ __forceinline__ void cv8_out(const CvTile& cur, const LAS unsigned char* T, int tid_) {
;     const int nbl = cur.N / 256, kb = cur.r / nbl, nb = cur.r - kb * nbl;
; #pragma unroll
;     for (int i = 0; i < 4; ++i) { const int p = tid_ + 512 * i, c = p & 7, n = p >> 3, nn = 256 * nb + n;
;         const int drow = (cur.mode == 0) ? nn : (256 * (nn >> 7) + (nn & 127) + (cur.mode == 2 ? 128 : 0));
;         const v4u w = *(const LAS v4u*)(T + n * 128 + 16 * (c ^ ((n >> 2) & 7)));
;         __builtin_nontemporal_store(w, (GAS v4u*)(cur.WT + (size_t)drow * cur.K + 128 * kb + 16 * c)); }
; }
.LBB0_481:
	s_waitcnt vmcnt(31)
	v_add_u32_e32 v66, s94, v132
	v_lshrrev_b32_e32 v0, 5, v66
	v_xor_b32_e32 v0, v0, v132
	v_lshlrev_b32_e32 v0, 4, v0
	v_and_b32_e32 v0, 0x70, v0
	v_add_u32_e32 v67, 0x200, v66
	v_add_u32_e32 v68, 0x400, v66
	v_add_u32_e32 v69, 0x600, v66
	s_waitcnt vmcnt(23)
	v_add_u32_e32 v101, 0, v0
	v_lshlrev_b32_e32 v0, 4, v132
	s_waitcnt vmcnt(22)
	v_ashrrev_i32_e32 v102, 3, v66
	v_ashrrev_i32_e32 v98, 3, v67
	v_ashrrev_i32_e32 v94, 3, v68
	v_ashrrev_i32_e32 v91, 3, v69
	v_and_b32_e32 v0, 0x70, v0
	v_and_b32_e32 v100, 0x7f, v102
	v_lshlrev_b32_e32 v99, 7, v102
	v_and_b32_e32 v97, 0x7f, v98
	v_lshlrev_b32_e32 v96, 7, v98
	v_and_b32_e32 v93, 0x7f, v94
	v_lshlrev_b32_e32 v92, 7, v94
	v_and_b32_e32 v90, 0x7f, v91
	v_lshlrev_b32_e32 v89, 7, v91
	s_andn2_b64 vcc, exec, s[40:41]
	s_ashr_i32 s57, s56, 31
	s_cbranch_vccnz .LBB0_484
	v_add_u32_e32 v70, v101, v99
	v_add_u32_e32 v71, v101, v96
	v_add_u32_e32 v72, v101, v92
	v_add_u32_e32 v73, v101, v89
	ds_read_b128 v[104:107], v70
	ds_read_b128 v[108:111], v71
	ds_read_b128 v[112:115], v72
	ds_read_b128 v[116:119], v73
	s_movk_i32 s2, 0x100
	s_movk_i32 s3, 0x140
	s_cmp_lg_u64 s[72:73], 0
	s_cselect_b32 s2, 0x80, s2
	s_cselect_b32 s3, 0xc0, s3
	v_add_u32_e32 v70, s84, v102
	v_lshlrev_b32_e32 v71, 1, v70
	v_and_b32_e32 v71, 0xffffff00, v71
	v_or3_b32 v71, v100, v71, s19
	v_cndmask_b32_e64 v76, v71, v70, s[72:73]
	v_ashrrev_i32_e32 v74, 31, v76
	v_mul_lo_u32 v78, s68, v74
	v_mov_b64_e32 v[74:75], s[66:67]
	v_mul_lo_u32 v79, s69, v76
	v_mad_u64_u32 v[76:77], s[0:1], s68, v76, v[74:75]
	s_lshl_b64 s[42:43], s[68:69], 6
	s_mul_i32 s44, s68, s2
	s_mul_hi_u32 s45, s68, s2
	s_mul_i32 s54, s69, s2
	s_add_i32 s45, s45, s54
	s_mul_i32 s46, s68, s3
	s_mul_hi_u32 s47, s68, s3
	s_mul_i32 s54, s69, s3
	s_add_i32 s47, s47, s54
	v_add3_u32 v77, v79, v77, v78
	v_lshl_add_u64 v[76:77], v[76:77], 0, s[56:57]
	v_lshl_add_u64 v[76:77], v[76:77], 0, v[0:1]
	s_mov_b64 s[14:15], 0
	s_and_b64 vcc, exec, s[74:75]
	v_lshl_add_u64 v[120:121], v[76:77], 0, s[42:43]
	v_lshl_add_u64 v[122:123], v[76:77], 0, s[44:45]
	v_lshl_add_u64 v[124:125], v[76:77], 0, s[46:47]
	s_waitcnt lgkmcnt(3)
	global_store_dwordx4 v[76:77], v[104:107], off nt
	s_waitcnt lgkmcnt(2)
	global_store_dwordx4 v[120:121], v[108:111], off nt
	s_waitcnt lgkmcnt(1)
	global_store_dwordx4 v[122:123], v[112:115], off nt
	s_mov_b64 s[0:1], 0
	s_waitcnt lgkmcnt(0)
	global_store_dwordx4 v[124:125], v[116:119], off nt
	s_cbranch_vccz .LBB0_485
	s_waitcnt lgkmcnt(0)
	s_mov_b64 s[0:1], -1
	s_barrier
	s_branch .LBB0_485

; #define GAS __attribute__((address_space(1)))
; #define LAS __attribute__((address_space(3)))
; __device__ __forceinline__ void cv8_out(const CvTile& cur, const LAS unsigned char* T, int tid_) {
;     const int nbl = cur.N / 256, kb = cur.r / nbl, nb = cur.r - kb * nbl;
; #pragma unroll
;     for (int i = 0; i < 4; ++i) { const int p = tid_ + 512 * i, c = p & 7, n = p >> 3, nn = 256 * nb + n;
;         const int drow = (cur.mode == 0) ? nn : (256 * (nn >> 7) + (nn & 127) + (cur.mode == 2 ? 128 : 0));
;         const v4u w = *(const LAS v4u*)(T + n * 128 + 16 * (c ^ ((n >> 2) & 7)));
;         __builtin_nontemporal_store(w, (GAS v4u*)(cur.WT + (size_t)drow * cur.K + 128 * kb + 16 * c)); }
; }
.LBB0_494:
	s_waitcnt vmcnt(13)
	v_add_u32_e32 v10, s22, v101
	v_add_u32_e32 v2, v10, v99
	v_add_u32_e32 v3, v10, v96
	v_add_u32_e32 v4, v10, v92
	v_add_u32_e32 v5, v10, v89
	ds_read_b128 v[16:19], v2
	ds_read_b128 v[20:23], v3
	ds_read_b128 v[24:27], v4
	ds_read_b128 v[28:31], v5
	s_movk_i32 s3, 0x100
	s_movk_i32 s4, 0x140
	s_cmp_lg_u64 s[62:63], 0
	s_cselect_b32 s3, 0x80, s3
	s_cselect_b32 s4, 0xc0, s4
	v_add_u32_e32 v2, s64, v102
	v_lshlrev_b32_e32 v3, 1, v2
	v_and_b32_e32 v3, 0xffffff00, v3
	v_or3_b32 v3, v100, v3, s18
	v_cndmask_b32_e64 v8, v3, v2, s[62:63]
	v_ashrrev_i32_e32 v6, 31, v8
	v_mul_lo_u32 v11, s60, v6
	v_mov_b64_e32 v[6:7], s[58:59]
	v_mul_lo_u32 v12, s61, v8
	v_mad_u64_u32 v[8:9], s[0:1], s60, v8, v[6:7]
	s_ashr_i32 s71, s70, 31
	s_lshl_b64 s[42:43], s[60:61], 6
	s_mul_i32 s44, s60, s3
	s_mul_hi_u32 s45, s60, s3
	s_mul_i32 s54, s61, s3
	s_add_i32 s45, s45, s54
	s_mul_i32 s46, s60, s4
	s_mul_hi_u32 s47, s60, s4
	s_mul_i32 s54, s61, s4
	s_add_i32 s47, s47, s54
	v_add3_u32 v9, v12, v9, v11
	v_lshl_add_u64 v[8:9], v[8:9], 0, s[70:71]
	v_lshl_add_u64 v[8:9], v[8:9], 0, v[0:1]
	v_lshl_add_u64 v[32:33], v[8:9], 0, s[42:43]
	v_lshl_add_u64 v[34:35], v[8:9], 0, s[44:45]
	v_lshl_add_u64 v[36:37], v[8:9], 0, s[46:47]
	s_waitcnt lgkmcnt(3)
	global_store_dwordx4 v[8:9], v[16:19], off nt
	s_waitcnt lgkmcnt(2)
	global_store_dwordx4 v[32:33], v[20:23], off nt
	s_waitcnt lgkmcnt(1)
	global_store_dwordx4 v[34:35], v[24:27], off nt
	s_waitcnt lgkmcnt(0)
	global_store_dwordx4 v[36:37], v[28:31], off nt
	s_waitcnt lgkmcnt(0)
	s_barrier
	s_cbranch_execz .LBB0_498
	s_branch .LBB0_499
